# placement: DSA attention loop head at offset 48 mod 64 (pads only; other loops unchanged)
# speedup vs baseline: 1.0042x; 1.0042x over previous
; #define VM_WAIT() asm volatile("s_waitcnt vmcnt(0)" ::: "memory")
; #define KDMA(k0, bf) do { const bf16_t* kb_ = Kh + (size_t)(k0) * D; _Pragma("unroll") for (int i_ = 0; i_ < 2; ++i_) pg8::glds16_s((const void*)kb_, koff[i_], ldsb + OFF_K + (bf) * SHM_K + wid * 1024 + i_ * 8192); } while (0)
; #define VDMA(k0, bf) do { const bf16_t* vb_ = Vh + (size_t)(k0) * D; _Pragma("unroll") for (int i_ = 0; i_ < 2; ++i_) pg8::glds16_s((const void*)vb_, voff[i_], ldsb + OFF_V + (bf) * SHM_V + wid * 1024 + i_ * 8192); } while (0)
; template <int MODE> ...
;     ...
;         f32x16 pA0, pA1, pB0, pB1; float mnA = 0.f, mnB = 0.f, alA = 1.f, alB = 1.f; bf16x8 pa0, pa1, pa2, pa3;
;         const int NTr = je - jb;
;         KDMA(jb * KVBLK, 0); VM_WAIT(); __syncthreads();
;         mw = MLOAD(jb); KDMA((jb + 1) * KVBLK, 1); VDMA(jb * KVBLK, 0);
;         if (ACT(jb)) { qkt<0, false>(pA0, pA1, lds, r32, hi, qr, qx); mask_bits(pA0, pA1, mw, hi); partialSM(pA0, pA1, m_reg, mnA, alA); }
;         VM_WAIT(); __syncthreads();
;     ...
;         const int tdiag = P0 / KVBLK; int r = 1;
;         for (; r + 1 < NTr && jb + r + 1 <= tdiag; r += 2) {
.LBB0_1158:
	s_cmp_eq_u32 s58, 1
	s_cselect_b32 s69, s3, s2
	s_lshl_b32 s1, s4, 2
	s_add_i32 s62, s1, 0
	s_add_i32 s62, s62, 0x11000
	v_lshlrev_b32_e32 v3, 1, v192
	v_lshlrev_b32_e32 v2, 4, v192
	v_and_b32_e32 v3, 32, v3
	s_movk_i32 s1, 0xc0
	s_cmp_lg_u32 0, -1
	v_and_or_b32 v2, v2, s1, v3
	s_cselect_b32 s1, 0, 0
	v_and_b32_e32 v3, 0x100, v36
	s_sub_i32 s2, s69, s61
	s_waitcnt vmcnt(0)
	s_add_i32 s33, s1, s72
	v_or3_b32 v2, v2, v3, v37
	s_add_i32 s70, s2, -1
	s_addk_i32 s33, 0x4000
	s_mov_b32 s26, 1
	v_add_u32_e32 v194, s1, v2
	s_cmp_lt_i32 s2, 3
	s_barrier
	s_cbranch_scc1 .LBB0_1175
	s_or_b32 s1, s61, 1
	s_cmp_ge_u32 s1, s71
	s_mov_b32 s74, 0
	s_cbranch_scc1 .LBB0_1177
	s_cmp_lg_u32 0, -1
	s_cselect_b32 s1, 0, 0
	s_add_i32 s1, s1, s72
	v_and_b32_e32 v2, 0x70, v199
	s_add_i32 s75, s1, 0x6000
	v_xad_u32 v18, v2, v207, 0
	v_xad_u32 v19, v203, v2, 0
	v_xad_u32 v20, v201, v2, 0
	v_xad_u32 v21, v200, v2, 0
	s_add_u32 s0, s45, s0
	v_mov_b32_e32 v16, v179
	v_mov_b32_e32 v17, v179
	s_addc_u32 s1, s46, 0
	v_mov_b32_e32 v2, v179
	v_mov_b32_e32 v3, v179
	v_mov_b32_e32 v4, v179
	v_mov_b32_e32 v5, v179
	v_mov_b32_e32 v6, v179
	v_mov_b32_e32 v7, v179
	v_mov_b32_e32 v8, v179
	v_mov_b32_e32 v9, v179
	v_mov_b32_e32 v10, v179
	v_mov_b32_e32 v11, v179
	v_mov_b32_e32 v12, v179
	v_mov_b32_e32 v13, v179
	v_mov_b32_e32 v14, v179
	v_mov_b32_e32 v15, v179
	v_add_u32_e32 v210, v18, v198
	v_add_u32_e32 v211, v19, v198
	v_add_u32_e32 v212, v20, v198
	v_add_u32_e32 v213, v21, v198
	v_mov_b64_e32 v[64:65], v[16:17]
	s_waitcnt vmcnt(0)
	v_mov_b64_e32 v[48:49], v[16:17]
	v_mov_b64_e32 v[32:33], v[16:17]
	v_cmp_gt_u32_e64 s[2:3], 32, v192
	v_lshl_add_u32 v208, v190, 2, s62
	v_add_u32_e32 v209, s62, v207
	v_lshl_add_u64 v[182:183], s[0:1], 0, v[178:179]
	v_mov_b32_e32 v181, 0
	s_mov_b64 s[0:1], s[18:19]
	s_mov_b64 s[6:7], s[20:21]
	v_mov_b32_e32 v214, v206
	v_mov_b64_e32 v[62:63], v[14:15]
	v_mov_b64_e32 v[60:61], v[12:13]
	v_mov_b64_e32 v[58:59], v[10:11]
	v_mov_b64_e32 v[56:57], v[8:9]
	v_mov_b64_e32 v[54:55], v[6:7]
	v_mov_b64_e32 v[52:53], v[4:5]
	v_mov_b64_e32 v[50:51], v[2:3]
	v_mov_b64_e32 v[46:47], v[14:15]
	v_mov_b64_e32 v[44:45], v[12:13]
	v_mov_b64_e32 v[42:43], v[10:11]
	v_mov_b64_e32 v[40:41], v[8:9]
	v_mov_b64_e32 v[38:39], v[6:7]
	v_mov_b64_e32 v[36:37], v[4:5]
	v_mov_b64_e32 v[34:35], v[2:3]
	v_mov_b64_e32 v[30:31], v[14:15]
	v_mov_b64_e32 v[28:29], v[12:13]
	v_mov_b64_e32 v[26:27], v[10:11]
	v_mov_b64_e32 v[24:25], v[8:9]
	v_mov_b64_e32 v[22:23], v[6:7]
	v_mov_b64_e32 v[20:21], v[4:5]
	v_mov_b64_e32 v[18:19], v[2:3]
	v_readfirstlane_b32 s99, v0
	s_nop 0
	s_lshr_b32 s99, s99, 8
	s_nop 0
	s_nop 0
	s_nop 0
	s_nop 0
	s_nop 0
	s_nop 0
	s_nop 0

; __device__ __forceinline__ void partialSM(f32x16& p0, f32x16& p1, float& m_reg, float& mn, float& alpha) {
;     ...
;     constexpr float C2 = 1.4426950408889634f * SCALE;
;     if (__builtin_expect(__all((pmax - m_reg) * SCALE <= THR), 1)) { mn = m_reg; alpha = 1.f; }
;     else { mn = fmaxf(m_reg, pmax); alpha = __builtin_amdgcn_exp2f((m_reg - mn) * C2); m_reg = mn; }
;     const float mnL = -mn * C2;
;     for (int r = 0; r < 16; ++r) p0[r] = fmaf(p0[r], C2, mnL); for (int r = 0; r < 16; ++r) p1[r] = fmaf(p1[r], C2, mnL);
;     for (int r = 0; r < 16; ++r) p0[r] = __builtin_amdgcn_exp2f(p0[r]);
.LBB0_1173:
	v_add_f32_e32 v185, v215, v216
	v_cndmask_b32_e64 v180, v129, v180, s[4:5]
	v_fmac_f32_e32 v185, v214, v181
	v_add_f32_e32 v181, v217, v218
	v_mul_f32_e32 v214, 0xbe0293ee, v180
	v_fmac_f32_e32 v181, v185, v195
	v_mov_b32_e32 v185, v214
	v_fmamk_f32 v98, v98, 0x3e0293ee, v214
	v_fmamk_f32 v99, v99, 0x3e0293ee, v214
	v_fmamk_f32 v100, v100, 0x3e0293ee, v214
	v_fmamk_f32 v101, v101, 0x3e0293ee, v214
	v_fmamk_f32 v102, v102, 0x3e0293ee, v214
	v_fmamk_f32 v103, v103, 0x3e0293ee, v214
	v_fmamk_f32 v104, v104, 0x3e0293ee, v214
	v_fmamk_f32 v105, v105, 0x3e0293ee, v214
	v_fmamk_f32 v106, v106, 0x3e0293ee, v214
	v_fmamk_f32 v107, v107, 0x3e0293ee, v214
	v_fmamk_f32 v108, v108, 0x3e0293ee, v214
	v_fmamk_f32 v109, v109, 0x3e0293ee, v214
	v_fmamk_f32 v110, v110, 0x3e0293ee, v214
	v_fmamk_f32 v111, v111, 0x3e0293ee, v214
	v_fmamk_f32 v184, v184, 0x3e0293ee, v214
	v_fmac_f32_e32 v185, 0x3e0293ee, v128
	v_pk_fma_f32 v[128:129], v[112:113], s[12:13], v[214:215] op_sel_hi:[1,0,0]
	v_exp_f32_e32 v98, v98
	v_exp_f32_e32 v99, v99
	v_exp_f32_e32 v100, v100
	v_exp_f32_e32 v101, v101
	v_exp_f32_e32 v102, v102
	v_exp_f32_e32 v103, v103
	v_exp_f32_e32 v104, v104
	v_exp_f32_e32 v105, v105
	v_exp_f32_e32 v106, v106
	v_exp_f32_e32 v107, v107
	v_exp_f32_e32 v108, v108
	v_exp_f32_e32 v109, v109
	v_exp_f32_e32 v110, v110
	v_exp_f32_e32 v111, v111
	v_exp_f32_e32 v112, v184
	v_exp_f32_e32 v113, v185
	v_pk_fma_f32 v[126:127], v[126:127], s[12:13], v[214:215] op_sel_hi:[1,0,0]
	v_pk_fma_f32 v[124:125], v[124:125], s[12:13], v[214:215] op_sel_hi:[1,0,0]
	v_pk_fma_f32 v[122:123], v[122:123], s[12:13], v[214:215] op_sel_hi:[1,0,0]
	v_pk_fma_f32 v[120:121], v[120:121], s[12:13], v[214:215] op_sel_hi:[1,0,0]
	v_pk_fma_f32 v[118:119], v[118:119], s[12:13], v[214:215] op_sel_hi:[1,0,0]
	v_pk_fma_f32 v[116:117], v[116:117], s[12:13], v[214:215] op_sel_hi:[1,0,0]
	v_pk_fma_f32 v[114:115], v[114:115], s[12:13], v[214:215] op_sel_hi:[1,0,0]
	s_andn2_b64 vcc, exec, s[26:27]
	s_cbranch_vccz .LBB0_1178
	v_mov_b32_e32 v214, v206
	s_branch .LBB0_1161
	s_nop 0
	s_nop 0
	s_nop 0
	s_nop 0
	s_nop 0
	s_nop 0
	s_nop 0
	s_nop 0
	s_nop 0
